# attention loop back-edge rotation: loop-carried moves, exit/rescale/sign-flip tests and ring-offset SALU in front of the loop-back barrier (on top of v66)
# speedup vs baseline: 1.0066x; 1.0066x over previous
.Lmy_x_reads:
	ds_read_b64_tr_b16 v[110:111], v2 offset:0
	ds_read_b64_tr_b16 v[112:113], v2 offset:0x800
	ds_read_b64_tr_b16 v[106:107], v2 offset:0x1000
	ds_read_b64_tr_b16 v[108:109], v2 offset:0x1800
	ds_read_b64_tr_b16 v[102:103], v2 offset:0x2000
	ds_read_b64_tr_b16 v[104:105], v2 offset:0x2800
	ds_read_b64_tr_b16 v[98:99], v2 offset:0x3000
	ds_read_b64_tr_b16 v[100:101], v2 offset:0x3800
	v_add_u32_e32 v12, s44, v225
	ds_read_b128 v[4:7], v12 offset:0
	ds_read_b128 v[8:11], v12 offset:0x2000
	v_add_u32_e32 v16, s44, v226
	ds_read_b128 v[170:173], v16 offset:0
	ds_read_b128 v[12:15], v16 offset:0x2000
	v_add_u32_e32 v16, s44, v227
	ds_read_b128 v[174:177], v16 offset:0
	ds_read_b128 v[162:165], v16 offset:0x2000
	v_add_u32_e32 v16, s44, v228
	ds_read_b128 v[178:181], v16 offset:0
	s_add_i32 s44, s38, 2
	ds_read_b128 v[166:169], v16 offset:0x2000
	s_cmp_ge_i32 s44, s35
	s_cselect_b64 s[96:97], -1, 0
	s_and_b64 vcc, exec, s[96:97]
	s_cbranch_vccnz .LBB0_534
	s_add_i32 s11, s34, s11
	v_lshl_add_u64 v[16:17], s[94:95], 0, v[208:209]
	s_add_i32 m0, s11, 0xc000
	s_nop 0
	global_load_lds_dwordx4 v[16:17], off
	v_lshl_add_u64 v[16:17], s[94:95], 0, v[210:211]
	s_add_i32 m0, s11, 0xc400
	s_nop 0
	global_load_lds_dwordx4 v[16:17], off

.LBB0_549:
	v_sub_f32_e32 v5, v233, v7
	v_exp_f32_e32 v5, v5
	s_add_i32 s31, s31, 64
	s_add_u32 s94, s94, 0xb0000
	v_add_f32_e32 v2, v4, v2
	v_cndmask_b32_e64 v98, v5, 1.0, s[10:11]
	s_addc_u32 s95, s95, 0
	v_fmac_f32_e32 v2, v231, v98
	s_cmp_eq_u32 s44, s35
	s_cbranch_scc1 .Lmy_rot_exit
	s_mov_b32 s55, s39
	s_mov_b32 s38, s44
	v_mov_b32_e32 v233, v6
	v_mov_b32_e32 v231, v2
	v_cmp_gt_f32_e32 vcc, 1.0, v98
	s_cbranch_vccnz .Lmy_rot_resc
	v_subrev_co_u32_e32 v234, vcc, 1, v234
	s_andn2_b64 vcc, exec, vcc
	s_cbranch_vccnz .Lmy_rot_noflip
	v_xor_b32 v18, 0x80000000, v18
	v_xor_b32 v19, 0x80000000, v19
	v_xor_b32 v20, 0x80000000, v20
	v_xor_b32 v21, 0x80000000, v21
	v_xor_b32 v22, 0x80000000, v22
	v_xor_b32 v23, 0x80000000, v23
	v_xor_b32 v24, 0x80000000, v24
	v_xor_b32 v25, 0x80000000, v25
	v_xor_b32 v26, 0x80000000, v26
	v_xor_b32 v27, 0x80000000, v27
	v_xor_b32 v28, 0x80000000, v28
	v_xor_b32 v29, 0x80000000, v29
	v_xor_b32 v30, 0x80000000, v30
	v_xor_b32 v31, 0x80000000, v31
	v_xor_b32 v32, 0x80000000, v32
	v_xor_b32 v33, 0x80000000, v33
.Lmy_rot_noflip:
	s_add_i32 s10, s55, 1
	s_cmp_lg_u32 s55, 2
	s_cselect_b32 s39, s10, 0
	s_lshl_b32 s10, s39, 14
	s_lshl_b32 s44, s55, 14
	s_add_i32 s11, s10, 0x4000
	s_cmp_lg_u32 s39, 2
	s_cselect_b32 s11, s11, 0
	v_add_u32_e32 v2, s11, v232
	s_barrier
	s_branch .Lmy_x_reads
.Lmy_rot_resc:
	s_barrier
	s_branch .LBB0_527
